# k_finalize tree: dropped the 7 barriers around wave-0-private steps and fused the last step with the final scale/store (on top of batched head loads)
# speedup vs baseline: 1.0118x; 1.0018x over previous
.LBB3_30:
	s_or_b64 exec, exec, s[2:3]
	v_cmp_gt_u32_e32 vcc, 32, v0
	s_waitcnt lgkmcnt(0)
	s_and_saveexec_b64 s[2:3], vcc
	s_cbranch_execz .LBB3_32
	ds_read2_b64 v[2:5], v1 offset1:32
	ds_read2_b64 v[8:11], v6 offset1:32
	s_waitcnt lgkmcnt(1)
	v_add_f64 v[2:3], v[4:5], v[2:3]
	s_waitcnt lgkmcnt(0)
	v_add_f64 v[4:5], v[10:11], v[8:9]
	ds_write_b64 v1, v[2:3]
	ds_write_b64 v6, v[4:5]
.LBB3_32:
	s_or_b64 exec, exec, s[2:3]
	v_cmp_gt_u32_e32 vcc, 16, v0
	s_waitcnt lgkmcnt(0)
	s_and_saveexec_b64 s[2:3], vcc
	s_cbranch_execz .LBB3_34
	ds_read2_b64 v[2:5], v1 offset1:16
	ds_read2_b64 v[8:11], v6 offset1:16
	s_waitcnt lgkmcnt(1)
	v_add_f64 v[2:3], v[4:5], v[2:3]
	s_waitcnt lgkmcnt(0)
	v_add_f64 v[4:5], v[10:11], v[8:9]
	ds_write_b64 v1, v[2:3]
	ds_write_b64 v6, v[4:5]
.LBB3_34:
	s_or_b64 exec, exec, s[2:3]
	v_cmp_gt_u32_e32 vcc, 8, v0
	s_waitcnt lgkmcnt(0)
	s_and_saveexec_b64 s[2:3], vcc
	s_cbranch_execz .LBB3_36
	ds_read2_b64 v[2:5], v1 offset1:8
	ds_read2_b64 v[8:11], v6 offset1:8
	s_waitcnt lgkmcnt(1)
	v_add_f64 v[2:3], v[4:5], v[2:3]
	s_waitcnt lgkmcnt(0)
	v_add_f64 v[4:5], v[10:11], v[8:9]
	ds_write_b64 v1, v[2:3]
	ds_write_b64 v6, v[4:5]
.LBB3_36:
	s_or_b64 exec, exec, s[2:3]
	v_cmp_gt_u32_e32 vcc, 4, v0
	s_waitcnt lgkmcnt(0)
	s_and_saveexec_b64 s[2:3], vcc
	s_cbranch_execz .LBB3_38
	ds_read2_b64 v[2:5], v1 offset1:4
	ds_read2_b64 v[8:11], v6 offset1:4
	s_waitcnt lgkmcnt(1)
	v_add_f64 v[2:3], v[4:5], v[2:3]
	s_waitcnt lgkmcnt(0)
	v_add_f64 v[4:5], v[10:11], v[8:9]
	ds_write_b64 v1, v[2:3]
	ds_write_b64 v6, v[4:5]
.LBB3_38:
	s_or_b64 exec, exec, s[2:3]
	v_cmp_gt_u32_e32 vcc, 2, v0
	s_waitcnt lgkmcnt(0)
	s_and_saveexec_b64 s[2:3], vcc
	s_cbranch_execz .LBB3_40
	ds_read2_b64 v[2:5], v1 offset1:2
	ds_read2_b64 v[8:11], v6 offset1:2
	s_waitcnt lgkmcnt(1)
	v_add_f64 v[2:3], v[4:5], v[2:3]
	s_waitcnt lgkmcnt(0)
	v_add_f64 v[4:5], v[10:11], v[8:9]
	ds_write_b64 v1, v[2:3]
	ds_write_b64 v6, v[4:5]
.LBB3_40:
	s_or_b64 exec, exec, s[2:3]
	v_cmp_eq_u32_e32 vcc, 0, v0
	s_waitcnt lgkmcnt(0)
	s_and_saveexec_b64 s[2:3], vcc
	s_cbranch_execz .LBB3_42
	v_add_u32_e64 v0, 8, 0
	ds_read2st64_b64 v[2:5], v0 offset1:16
	ds_read_b64 v[8:9], v1
	ds_read_b64 v[10:11], v6
	s_waitcnt lgkmcnt(1)
	v_add_f64 v[2:3], v[2:3], v[8:9]
	s_waitcnt lgkmcnt(0)
	v_add_f64 v[4:5], v[4:5], v[10:11]
	s_movk_i32 s4, 0xffe6
	s_movk_i32 s5, 0xffe9
	v_ldexp_f64 v[0:1], v[2:3], s4
	v_ldexp_f64 v[2:3], v[4:5], s5
	v_cvt_f32_f64_e32 v1, v[0:1]
	v_cvt_f32_f64_e32 v0, v[2:3]
	v_fmamk_f32 v2, v0, 0x3e800000, v0
	v_add_f32_e32 v0, v2, v1
	v_mov_b32_e32 v4, 0
	global_store_dwordx3 v4, v[0:2], s[0:1]
